# routed-expert queues: first claim of a phase is the workgroup's own index (no atomic), later claims gridDim + atomicAdd
# baseline (speedup 1.0000x reference)
.LBB0_1279:
	s_cmp_le_i32 s74, s2
	s_cselect_b64 s[2:3], -1, 0
	s_and_b64 s[0:1], s[2:3], s[0:1]
	v_writelane_b32 v255, s0, 11
	s_andn2_b64 vcc, exec, s[0:1]
	s_nop 0
	v_writelane_b32 v255, s1, 12
	s_cbranch_vccnz .LBB0_1346
	v_readlane_b32 s0, v254, 41
	v_readlane_b32 s2, v254, 60
	v_readlane_b32 s3, v254, 61
	v_mov_b32_e32 v0, s0
	s_waitcnt vmcnt(0)
	ds_read_b64 v[2:3], v0
	s_mov_b32 s3, s57
	s_lshl_b32 s56, s2, 13
	s_lshl_b32 s0, s2, 8
	v_writelane_b32 v254, s2, 60
	s_waitcnt lgkmcnt(0)
	v_readfirstlane_b32 s15, v2
	s_lshl_b64 s[8:9], s[56:57], 2
	v_writelane_b32 v254, s3, 61
	s_lshl_b64 s[2:3], s[2:3], 28
	v_readfirstlane_b32 s16, v3
	s_add_u32 s8, s15, s8
	v_readlane_b32 s11, v253, 0
	s_addc_u32 s9, s16, s9
	v_mbcnt_lo_u32_b32 v0, -1, 0
	v_mbcnt_hi_u32_b32 v0, -1, v0
	s_mov_b32 s1, s57
	v_add_u32_e32 v231, s11, v0
	s_add_u32 s50, s8, 0x10000
	v_readfirstlane_b32 s8, v231
	s_addc_u32 s51, s9, 0
	s_ashr_i32 s9, s8, 6
	s_lshl_b64 s[18:19], s[0:1], 2
	s_add_u32 s0, s15, s18
	v_writelane_b32 v255, s18, 13
	s_addc_u32 s1, s16, s19
	s_add_u32 s52, s0, 0xa000
	s_addc_u32 s53, s1, 0
	v_readlane_b32 s11, v254, 53
	v_writelane_b32 v255, s19, 14
	s_add_u32 s0, s15, 0x2e3e0000
	v_mov_b32_e32 v0, s11
	v_writelane_b32 v255, s0, 15
	s_addc_u32 s0, s16, 0
	ds_read_b128 v[2:5], v0
	s_add_u32 s54, s15, 0x4ffe0a00
	s_addc_u32 s55, s16, 0
	s_add_u32 s58, s15, 0x2f3e0000
	v_writelane_b32 v255, s0, 16
	s_addc_u32 s59, s16, 0
	s_ashr_i32 s0, s8, 7
	s_and_b32 s1, s9, 1
	v_writelane_b32 v255, s15, 17
	s_lshl_b32 s28, s0, 5
	s_lshl_b32 s15, s1, 5
	s_waitcnt lgkmcnt(0)
	v_readfirstlane_b32 s11, v2
	v_readfirstlane_b32 s13, v4
	s_cmp_lt_i32 s0, 2
	v_readfirstlane_b32 s12, v3
	v_readfirstlane_b32 s14, v5
	s_cselect_b32 s11, s11, s13
	s_cselect_b32 s0, s12, s14
	s_add_u32 s2, s11, s2
	v_writelane_b32 v255, s16, 18
	s_addc_u32 s0, s0, s3
	s_lshl_b32 s3, s9, 8
	v_writelane_b32 v255, s15, 5
	s_add_i32 s3, s3, 0
	v_writelane_b32 v255, s3, 7
	s_and_b32 s3, s8, 0x80
	s_add_u32 s2, s2, s3
	s_addc_u32 s0, s0, 0
	s_and_b32 s83, s8, 0xffffffc0
	v_writelane_b32 v255, s2, 19
	s_lshl_b32 s2, s83, 2
	s_add_i32 s87, s2, 0
	s_ashr_i32 s2, s8, 8
	v_writelane_b32 v255, s0, 20
	s_lshl_b32 s0, s9, 5
	s_lshl_b32 s3, s2, 13
	s_and_b32 s0, s0, 0xffffff80
	s_add_i32 s3, s3, 0
	s_lshl_b32 s1, s1, 12
	s_add_i32 s0, s0, 0
	s_add_i32 s78, s3, s1
	v_writelane_b32 v255, s0, 9
	s_and_b32 s0, s9, 3
	s_or_b32 s80, s83, 32
	s_add_i32 s78, s78, 0x10000
	s_cmp_gt_u32 s0, 1
	s_cselect_b64 s[60:61], -1, 0
	s_cmp_lt_u32 s0, 2
	s_mul_i32 s33, s0, 0x1200
	s_cselect_b64 s[62:63], -1, 0
	s_lshl_b32 s64, s0, 5
	s_lshl_b32 s0, s9, 4
	s_and_b32 s0, s0, 16
	v_cmp_eq_u32_e64 s[18:19], 0, v231
	v_writelane_b32 v255, s0, 3
	s_lshl_b32 s1, s2, 7
	v_writelane_b32 v255, s18, 21
	s_add_i32 s3, s1, 0
	s_mov_b32 s65, s57
	v_writelane_b32 v255, s19, 22
	v_readlane_b32 s36, v253, 3
	v_readlane_b32 s37, v253, 4
	s_load_dword s36, s[36:37], 0x0
	s_waitcnt lgkmcnt(0)
	v_writelane_b32 v252, s36, 11
	s_mov_b32 s36, 1
	s_nop 0
	v_writelane_b32 v252, s36, 10
	s_branch .LBB0_1283

.LBB0_1286:
	s_mov_b32 s37, 0
	s_mov_b64 s[14:15], exec
	v_mbcnt_lo_u32_b32 v0, s14, 0
	v_mbcnt_hi_u32_b32 v0, s15, v0
	v_cmp_eq_u32_e32 vcc, 0, v0
	s_and_saveexec_b64 s[12:13], vcc
	s_cbranch_execz .LBB0_1288
	v_readlane_b32 s36, v252, 10
	v_readlane_b32 s37, v252, 11
	s_cmp_eq_u32 s36, 0
	s_cbranch_scc1 .Lq_dyn_s2
	v_writelane_b32 v252, s57, 10
	v_readlane_b32 s36, v254, 32
	s_mov_b32 s37, 0
	s_nop 0
	v_mov_b32_e32 v2, s36
	s_branch .LBB0_1288
.Lq_dyn_s2:
	s_bcnt1_i32_b64 s2, s[14:15]
	v_mov_b32_e32 v2, s2
	global_atomic_add v2, v1, v2, s[52:53] sc0
.LBB0_1288:
	s_or_b64 exec, exec, s[12:13]
	s_waitcnt vmcnt(0)
	v_readfirstlane_b32 s2, v2
	s_mov_b64 s[14:15], -1
	s_nop 0
	s_add_i32 s2, s2, s37
	s_nop 0
	v_add_u32_e32 v2, s2, v0
	v_add_u32_e32 v0, 0xffffff00, v2
	s_movk_i32 s2, 0x400
	v_cmp_gt_u32_e32 vcc, s2, v0
	s_and_saveexec_b64 s[12:13], vcc
	s_cbranch_execz .LBB0_1285
	v_lshlrev_b32_e32 v0, 5, v2
	v_and_b32_e32 v0, 0xff80, v0
	v_lshl_add_u64 v[4:5], s[50:51], 0, v[0:1]
	v_add_co_u32_e32 v4, vcc, 0xffffe000, v4
	s_movk_i32 s2, 0x240
	s_nop 0
	v_addc_co_u32_e32 v5, vcc, -1, v5, vcc
	global_load_dword v0, v[4:5], off
	s_waitcnt vmcnt(0)
	v_cmp_lt_i32_e32 vcc, s2, v0
	s_orn2_b64 s[14:15], vcc, exec
	s_branch .LBB0_1285

.LBB0_1402:
	s_cmp_le_i32 s74, s2
	s_cselect_b64 s[2:3], -1, 0
	s_and_b64 s[8:9], s[2:3], s[0:1]
	s_andn2_b64 vcc, exec, s[8:9]
	s_cbranch_vccnz .LBB0_1456
	v_readlane_b32 s2, v254, 60
	v_readlane_b32 s0, v254, 41
	v_readlane_b32 s3, v254, 61
	s_mov_b32 s3, s57
	v_mov_b32_e32 v0, s0
	s_waitcnt vmcnt(0)
	ds_read_b64 v[2:3], v0
	s_lshl_b32 s56, s2, 13
	s_lshl_b64 s[12:13], s[2:3], 28
	v_writelane_b32 v254, s2, 60
	v_readlane_b32 s11, v253, 0
	v_mbcnt_lo_u32_b32 v0, -1, 0
	v_mbcnt_hi_u32_b32 v0, -1, v0
	s_lshl_b32 s0, s2, 8
	v_writelane_b32 v254, s3, 61
	v_add_u32_e32 v231, s11, v0
	v_readlane_b32 s11, v254, 55
	s_waitcnt lgkmcnt(0)
	v_readfirstlane_b32 s2, v2
	v_readfirstlane_b32 s3, v3
	v_mov_b32_e32 v0, s11
	ds_read_b64 v[2:3], v0
	s_or_b32 s14, s0, 64
	s_lshl_b64 s[0:1], s[56:57], 2
	s_add_u32 s0, s2, s0
	s_addc_u32 s1, s3, s1
	s_add_u32 s0, s0, 0x10000
	v_readfirstlane_b32 s33, v231
	s_addc_u32 s1, s1, 0
	s_ashr_i32 s25, s33, 6
	s_waitcnt lgkmcnt(0)
	v_readfirstlane_b32 s11, v2
	s_mov_b32 s15, s57
	v_readfirstlane_b32 s16, v3
	s_add_u32 s27, s11, s12
	s_addc_u32 s34, s16, s13
	s_lshl_b64 s[14:15], s[14:15], 2
	s_add_u32 s11, s2, s14
	s_addc_u32 s12, s3, s15
	s_add_u32 s16, s11, 0xa000
	s_addc_u32 s17, s12, 0
	s_add_u32 s11, s2, 0x2e3e0000
	s_addc_u32 s26, s3, 0
	s_add_u32 s18, s2, 0x2e360000
	s_addc_u32 s19, s3, 0
	s_add_u32 s30, s2, 0x2f3e0000
	s_addc_u32 s31, s3, 0
	s_add_u32 s12, s2, 0x33be0200
	s_addc_u32 s13, s3, 0
	s_lshl_b32 s28, s25, 4
	v_bfe_u32 v3, v231, 3, 3
	v_and_b32_e32 v2, 7, v231
	v_and_or_b32 v3, s28, 16, v3
	s_andn2_b32 s28, s28, 31
	v_lshlrev_b32_e32 v4, 4, v2
	v_or_b32_e32 v2, s28, v2
	s_movk_i32 s35, 0x90
	s_ashr_i32 s29, s28, 31
	v_mul_lo_u32 v2, v2, s35
	s_lshl_b32 s35, s25, 8
	s_add_i32 s35, s35, 0
	s_lshl_b64 s[28:29], s[28:29], 2
	s_add_u32 s27, s27, s28
	s_addc_u32 s28, s34, s29
	s_lshl_b32 s34, s25, 5
	v_and_b32_e32 v0, 31, v231
	s_and_b32 s29, s34, 0xffffff80
	v_and_b32_e32 v232, 32, v231
	v_lshl_add_u32 v234, v3, 2, v2
	v_mul_u32_u24_e32 v2, 0x48, v0
	v_lshlrev_b32_e32 v0, 2, v0
	s_add_i32 s29, s29, 0
	s_andn2_b32 s33, s33, 63
	s_and_b32 s38, s25, 3
	v_cmp_eq_u32_e64 s[40:41], 0, v231
	v_lshl_or_b32 v233, v3, 13, v4
	v_add_lshl_u32 v235, v2, v232, 1
	v_add_u32_e32 v236, s35, v0
	v_add_u32_e32 v237, s29, v0
	s_mulk_i32 s38, 0x1200
	s_or_b32 s39, s33, 32
	s_and_b32 s34, s34, 0x60
	s_mov_b32 s35, s57
	v_readlane_b32 s98, v253, 3
	v_readlane_b32 s99, v253, 4
	s_load_dword s98, s[98:99], 0x0
	s_waitcnt lgkmcnt(0)
	v_writelane_b32 v252, s98, 11
	s_mov_b32 s98, 1
	s_nop 0
	v_writelane_b32 v252, s98, 10
	s_branch .LBB0_1406

.LBB0_1409:
	s_mov_b32 s99, 0
	s_mov_b64 s[46:47], exec
	v_mbcnt_lo_u32_b32 v0, s46, 0
	v_mbcnt_hi_u32_b32 v0, s47, v0
	v_cmp_eq_u32_e32 vcc, 0, v0
	s_and_saveexec_b64 s[44:45], vcc
	s_cbranch_execz .LBB0_1411
	v_readlane_b32 s98, v252, 10
	v_readlane_b32 s99, v252, 11
	s_cmp_eq_u32 s98, 0
	s_cbranch_scc1 .Lq_dyn_s25
	v_writelane_b32 v252, s57, 10
	v_readlane_b32 s98, v254, 32
	s_mov_b32 s99, 0
	s_nop 0
	v_mov_b32_e32 v2, s98
	s_branch .LBB0_1411
.Lq_dyn_s25:
	s_bcnt1_i32_b64 s25, s[46:47]
	v_mov_b32_e32 v2, s25
	global_atomic_add v2, v1, v2, s[16:17] sc0
.LBB0_1411:
	s_or_b64 exec, exec, s[44:45]
	s_waitcnt vmcnt(0)
	v_readfirstlane_b32 s25, v2
	s_mov_b64 s[46:47], -1
	s_nop 0
	s_add_i32 s25, s25, s99
	s_nop 0
	v_add_u32_e32 v2, s25, v0
	v_add_u32_e32 v0, 0xffffff00, v2
	s_movk_i32 s25, 0x400
	v_cmp_gt_u32_e32 vcc, s25, v0
	s_and_saveexec_b64 s[44:45], vcc
	s_cbranch_execz .LBB0_1408
	v_lshlrev_b32_e32 v0, 5, v2
	v_and_b32_e32 v0, 0xff80, v0
	v_lshl_add_u64 v[4:5], s[0:1], 0, v[0:1]
	v_add_co_u32_e32 v4, vcc, 0xffffe000, v4
	s_movk_i32 s25, 0x240
	s_nop 0
	v_addc_co_u32_e32 v5, vcc, -1, v5, vcc
	global_load_dword v0, v[4:5], off
	s_waitcnt vmcnt(0)
	v_cmp_lt_i32_e32 vcc, s25, v0
	s_orn2_b64 s[46:47], vcc, exec
	s_branch .LBB0_1408
